# speedup vs baseline: 1.0467x; 1.0108x over previous
.LBB1_6:
	s_mul_i32 s18, s33, 0xc0
	s_barrier
	v_and_b32_e32 v110, 15, v0
	v_bfe_u32 v111, v0, 4, 2
	s_lshl_b32 s52, s40, 5
	v_or_b32_e32 v112, s52, v110
	v_mul_u32_u24_e32 v113, 0x90, v112
	v_lshl_add_u32 v113, v111, 3, v113
	v_bfe_u32 v114, v0, 2, 1
	v_bfe_u32 v115, v0, 3, 1
	v_lshlrev_b32_e32 v114, 3, v114
	v_lshl_or_b32 v114, v115, 2, v114
	v_and_b32_e32 v115, 3, v0
	v_or_b32_e32 v114, v114, v115
	v_or_b32_e32 v114, s52, v114
	v_lshlrev_b32_e32 v114, 1, v114
	v_mul_u32_u24_e32 v115, 0x840, v111
	v_add_u32_e32 v114, v114, v115
	v_mov_b32_e32 v116, 0x3e38aa3b
	v_mov_b32_e32 v117, 0x3e38aa3b
	s_add_i32 s53, s37, 0
	s_add_i32 s54, s53, s18
	s_lshr_b32 s55, s54, 10
	s_lshr_b32 s56, s53, 6
	s_mul_i32 s56, s56, 0x9000
	s_and_b32 s57, s53, 63
	v_pk_add_f32 v[98:99], v[188:189], v[98:99]
	v_pk_add_f32 v[100:101], v[190:191], v[100:101]
	v_pk_add_f32 v[90:91], v[188:189], v[90:91]
	v_pk_add_f32 v[92:93], v[190:191], v[92:93]
	v_pk_add_f32 v[86:87], v[188:189], v[86:87]
	v_pk_add_f32 v[88:89], v[190:191], v[88:89]
	v_pk_add_f32 v[82:83], v[188:189], v[82:83]
	v_pk_add_f32 v[84:85], v[190:191], v[84:85]
	s_cmp_eq_u32 s55, 2
	s_cbranch_scc1 .Lmy_qe0_v
	s_lshl_b32 s58, s57, 1
	s_add_i32 s58, s58, s56
	v_add_u32_e32 v118, s58, v113
	s_cmp_eq_u32 s55, 0
	s_cbranch_scc0 .Lmy_qe0_ns
	v_pk_mul_f32 v[98:99], v[116:117], v[98:99]
	v_pk_mul_f32 v[100:101], v[116:117], v[100:101]
	v_pk_mul_f32 v[90:91], v[116:117], v[90:91]
	v_pk_mul_f32 v[92:93], v[116:117], v[92:93]
	v_pk_mul_f32 v[86:87], v[116:117], v[86:87]
	v_pk_mul_f32 v[88:89], v[116:117], v[88:89]
	v_pk_mul_f32 v[82:83], v[116:117], v[82:83]
	v_pk_mul_f32 v[84:85], v[116:117], v[84:85]
.Lmy_qe0_ns:
	v_cvt_pk_f16_f32 v120, v98, v99
	v_cvt_pk_f16_f32 v121, v100, v101
	v_cvt_pk_f16_f32 v122, v90, v91
	v_cvt_pk_f16_f32 v123, v92, v93
	v_cvt_pk_f16_f32 v124, v86, v87
	v_cvt_pk_f16_f32 v125, v88, v89
	v_cvt_pk_f16_f32 v126, v82, v83
	v_cvt_pk_f16_f32 v127, v84, v85
	ds_write_b64 v118, v[120:121]
	ds_write_b64 v118, v[122:123] offset:2304
	ds_write_b64 v118, v[124:125] offset:18432
	ds_write_b64 v118, v[126:127] offset:20736
	s_branch .Lmy_qe0_end
.Lmy_qe0_v:
	s_mul_i32 s58, s57, 0x210
	s_add_i32 s58, s58, s56
	v_add_u32_e32 v118, s58, v114
	v_cvt_pk_f16_f32 v120, v98, v99
	v_cvt_pk_f16_f32 v121, v100, v101
	v_cvt_pk_f16_f32 v122, v90, v91
	v_cvt_pk_f16_f32 v123, v92, v93
	v_cvt_pk_f16_f32 v124, v86, v87
	v_cvt_pk_f16_f32 v125, v88, v89
	v_cvt_pk_f16_f32 v126, v82, v83
	v_cvt_pk_f16_f32 v127, v84, v85
	ds_write_b16 v118, v120
	ds_write_b16_d16_hi v118, v120 offset:528
	ds_write_b16 v118, v121 offset:1056
	ds_write_b16_d16_hi v118, v121 offset:1584
	ds_write_b16 v118, v122 offset:32
	ds_write_b16_d16_hi v118, v122 offset:560
	ds_write_b16 v118, v123 offset:1088
	ds_write_b16_d16_hi v118, v123 offset:1616
	ds_write_b16 v118, v124 offset:256
	ds_write_b16_d16_hi v118, v124 offset:784
	ds_write_b16 v118, v125 offset:1312
	ds_write_b16_d16_hi v118, v125 offset:1840
	ds_write_b16 v118, v126 offset:288
	ds_write_b16_d16_hi v118, v126 offset:816
	ds_write_b16 v118, v127 offset:1344
	ds_write_b16_d16_hi v118, v127 offset:1872
.Lmy_qe0_end:
	s_add_i32 s53, s37, 16
	s_add_i32 s54, s53, s18
	s_lshr_b32 s55, s54, 10
	s_lshr_b32 s56, s53, 6
	s_mul_i32 s56, s56, 0x9000
	s_and_b32 s57, s53, 63
	v_pk_add_f32 v[78:79], v[192:193], v[78:79]
	v_pk_add_f32 v[80:81], v[194:195], v[80:81]
	v_pk_add_f32 v[74:75], v[192:193], v[74:75]
	v_pk_add_f32 v[76:77], v[194:195], v[76:77]
	v_pk_add_f32 v[70:71], v[192:193], v[70:71]
	v_pk_add_f32 v[72:73], v[194:195], v[72:73]
	v_pk_add_f32 v[66:67], v[192:193], v[66:67]
	v_pk_add_f32 v[68:69], v[194:195], v[68:69]
	s_cmp_eq_u32 s55, 2
	s_cbranch_scc1 .Lmy_qe1_v
	s_lshl_b32 s58, s57, 1
	s_add_i32 s58, s58, s56
	v_add_u32_e32 v118, s58, v113
	s_cmp_eq_u32 s55, 0
	s_cbranch_scc0 .Lmy_qe1_ns
	v_pk_mul_f32 v[78:79], v[116:117], v[78:79]
	v_pk_mul_f32 v[80:81], v[116:117], v[80:81]
	v_pk_mul_f32 v[74:75], v[116:117], v[74:75]
	v_pk_mul_f32 v[76:77], v[116:117], v[76:77]
	v_pk_mul_f32 v[70:71], v[116:117], v[70:71]
	v_pk_mul_f32 v[72:73], v[116:117], v[72:73]
	v_pk_mul_f32 v[66:67], v[116:117], v[66:67]
	v_pk_mul_f32 v[68:69], v[116:117], v[68:69]
.Lmy_qe1_ns:
	v_cvt_pk_f16_f32 v120, v78, v79
	v_cvt_pk_f16_f32 v121, v80, v81
	v_cvt_pk_f16_f32 v122, v74, v75
	v_cvt_pk_f16_f32 v123, v76, v77
	v_cvt_pk_f16_f32 v124, v70, v71
	v_cvt_pk_f16_f32 v125, v72, v73
	v_cvt_pk_f16_f32 v126, v66, v67
	v_cvt_pk_f16_f32 v127, v68, v69
	ds_write_b64 v118, v[120:121]
	ds_write_b64 v118, v[122:123] offset:2304
	ds_write_b64 v118, v[124:125] offset:18432
	ds_write_b64 v118, v[126:127] offset:20736
	s_branch .Lmy_qe1_end
.Lmy_qe1_v:
	s_mul_i32 s58, s57, 0x210
	s_add_i32 s58, s58, s56
	v_add_u32_e32 v118, s58, v114
	v_cvt_pk_f16_f32 v120, v78, v79
	v_cvt_pk_f16_f32 v121, v80, v81
	v_cvt_pk_f16_f32 v122, v74, v75
	v_cvt_pk_f16_f32 v123, v76, v77
	v_cvt_pk_f16_f32 v124, v70, v71
	v_cvt_pk_f16_f32 v125, v72, v73
	v_cvt_pk_f16_f32 v126, v66, v67
	v_cvt_pk_f16_f32 v127, v68, v69
	ds_write_b16 v118, v120
	ds_write_b16_d16_hi v118, v120 offset:528
	ds_write_b16 v118, v121 offset:1056
	ds_write_b16_d16_hi v118, v121 offset:1584
	ds_write_b16 v118, v122 offset:32
	ds_write_b16_d16_hi v118, v122 offset:560
	ds_write_b16 v118, v123 offset:1088
	ds_write_b16_d16_hi v118, v123 offset:1616
	ds_write_b16 v118, v124 offset:256
	ds_write_b16_d16_hi v118, v124 offset:784
	ds_write_b16 v118, v125 offset:1312
	ds_write_b16_d16_hi v118, v125 offset:1840
	ds_write_b16 v118, v126 offset:288
	ds_write_b16_d16_hi v118, v126 offset:816
	ds_write_b16 v118, v127 offset:1344
	ds_write_b16_d16_hi v118, v127 offset:1872
.Lmy_qe1_end:
	s_add_i32 s53, s37, 32
	s_add_i32 s54, s53, s18
	s_lshr_b32 s55, s54, 10
	s_lshr_b32 s56, s53, 6
	s_mul_i32 s56, s56, 0x9000
	s_and_b32 s57, s53, 63
	v_pk_add_f32 v[62:63], v[196:197], v[62:63]
	v_pk_add_f32 v[64:65], v[198:199], v[64:65]
	v_pk_add_f32 v[58:59], v[196:197], v[58:59]
	v_pk_add_f32 v[60:61], v[198:199], v[60:61]
	v_pk_add_f32 v[54:55], v[196:197], v[54:55]
	v_pk_add_f32 v[56:57], v[198:199], v[56:57]
	v_pk_add_f32 v[50:51], v[196:197], v[50:51]
	v_pk_add_f32 v[52:53], v[198:199], v[52:53]
	s_cmp_eq_u32 s55, 2
	s_cbranch_scc1 .Lmy_qe2_v
	s_lshl_b32 s58, s57, 1
	s_add_i32 s58, s58, s56
	v_add_u32_e32 v118, s58, v113
	s_cmp_eq_u32 s55, 0
	s_cbranch_scc0 .Lmy_qe2_ns
	v_pk_mul_f32 v[62:63], v[116:117], v[62:63]
	v_pk_mul_f32 v[64:65], v[116:117], v[64:65]
	v_pk_mul_f32 v[58:59], v[116:117], v[58:59]
	v_pk_mul_f32 v[60:61], v[116:117], v[60:61]
	v_pk_mul_f32 v[54:55], v[116:117], v[54:55]
	v_pk_mul_f32 v[56:57], v[116:117], v[56:57]
	v_pk_mul_f32 v[50:51], v[116:117], v[50:51]
	v_pk_mul_f32 v[52:53], v[116:117], v[52:53]
.Lmy_qe2_ns:
	v_cvt_pk_f16_f32 v120, v62, v63
	v_cvt_pk_f16_f32 v121, v64, v65
	v_cvt_pk_f16_f32 v122, v58, v59
	v_cvt_pk_f16_f32 v123, v60, v61
	v_cvt_pk_f16_f32 v124, v54, v55
	v_cvt_pk_f16_f32 v125, v56, v57
	v_cvt_pk_f16_f32 v126, v50, v51
	v_cvt_pk_f16_f32 v127, v52, v53
	ds_write_b64 v118, v[120:121]
	ds_write_b64 v118, v[122:123] offset:2304
	ds_write_b64 v118, v[124:125] offset:18432
	ds_write_b64 v118, v[126:127] offset:20736
	s_branch .Lmy_qe2_end
.Lmy_qe2_v:
	s_mul_i32 s58, s57, 0x210
	s_add_i32 s58, s58, s56
	v_add_u32_e32 v118, s58, v114
	v_cvt_pk_f16_f32 v120, v62, v63
	v_cvt_pk_f16_f32 v121, v64, v65
	v_cvt_pk_f16_f32 v122, v58, v59
	v_cvt_pk_f16_f32 v123, v60, v61
	v_cvt_pk_f16_f32 v124, v54, v55
	v_cvt_pk_f16_f32 v125, v56, v57
	v_cvt_pk_f16_f32 v126, v50, v51
	v_cvt_pk_f16_f32 v127, v52, v53
	ds_write_b16 v118, v120
	ds_write_b16_d16_hi v118, v120 offset:528
	ds_write_b16 v118, v121 offset:1056
	ds_write_b16_d16_hi v118, v121 offset:1584
	ds_write_b16 v118, v122 offset:32
	ds_write_b16_d16_hi v118, v122 offset:560
	ds_write_b16 v118, v123 offset:1088
	ds_write_b16_d16_hi v118, v123 offset:1616
	ds_write_b16 v118, v124 offset:256
	ds_write_b16_d16_hi v118, v124 offset:784
	ds_write_b16 v118, v125 offset:1312
	ds_write_b16_d16_hi v118, v125 offset:1840
	ds_write_b16 v118, v126 offset:288
	ds_write_b16_d16_hi v118, v126 offset:816
	ds_write_b16 v118, v127 offset:1344
	ds_write_b16_d16_hi v118, v127 offset:1872
.Lmy_qe2_end:
	s_add_i32 s53, s37, 96
	s_add_i32 s54, s53, s18
	s_lshr_b32 s55, s54, 10
	s_lshr_b32 s56, s53, 6
	s_mul_i32 s56, s56, 0x9000
	s_and_b32 s57, s53, 63
	v_pk_add_f32 v[46:47], v[200:201], v[46:47]
	v_pk_add_f32 v[48:49], v[202:203], v[48:49]
	v_pk_add_f32 v[42:43], v[200:201], v[42:43]
	v_pk_add_f32 v[44:45], v[202:203], v[44:45]
	v_pk_add_f32 v[38:39], v[200:201], v[38:39]
	v_pk_add_f32 v[40:41], v[202:203], v[40:41]
	v_pk_add_f32 v[34:35], v[200:201], v[34:35]
	v_pk_add_f32 v[36:37], v[202:203], v[36:37]
	s_cmp_eq_u32 s55, 2
	s_cbranch_scc1 .Lmy_qe3_v
	s_lshl_b32 s58, s57, 1
	s_add_i32 s58, s58, s56
	v_add_u32_e32 v118, s58, v113
	s_cmp_eq_u32 s55, 0
	s_cbranch_scc0 .Lmy_qe3_ns
	v_pk_mul_f32 v[46:47], v[116:117], v[46:47]
	v_pk_mul_f32 v[48:49], v[116:117], v[48:49]
	v_pk_mul_f32 v[42:43], v[116:117], v[42:43]
	v_pk_mul_f32 v[44:45], v[116:117], v[44:45]
	v_pk_mul_f32 v[38:39], v[116:117], v[38:39]
	v_pk_mul_f32 v[40:41], v[116:117], v[40:41]
	v_pk_mul_f32 v[34:35], v[116:117], v[34:35]
	v_pk_mul_f32 v[36:37], v[116:117], v[36:37]
.Lmy_qe3_ns:
	v_cvt_pk_f16_f32 v120, v46, v47
	v_cvt_pk_f16_f32 v121, v48, v49
	v_cvt_pk_f16_f32 v122, v42, v43
	v_cvt_pk_f16_f32 v123, v44, v45
	v_cvt_pk_f16_f32 v124, v38, v39
	v_cvt_pk_f16_f32 v125, v40, v41
	v_cvt_pk_f16_f32 v126, v34, v35
	v_cvt_pk_f16_f32 v127, v36, v37
	ds_write_b64 v118, v[120:121]
	ds_write_b64 v118, v[122:123] offset:2304
	ds_write_b64 v118, v[124:125] offset:18432
	ds_write_b64 v118, v[126:127] offset:20736
	s_branch .Lmy_qe3_end
.Lmy_qe3_v:
	s_mul_i32 s58, s57, 0x210
	s_add_i32 s58, s58, s56
	v_add_u32_e32 v118, s58, v114
	v_cvt_pk_f16_f32 v120, v46, v47
	v_cvt_pk_f16_f32 v121, v48, v49
	v_cvt_pk_f16_f32 v122, v42, v43
	v_cvt_pk_f16_f32 v123, v44, v45
	v_cvt_pk_f16_f32 v124, v38, v39
	v_cvt_pk_f16_f32 v125, v40, v41
	v_cvt_pk_f16_f32 v126, v34, v35
	v_cvt_pk_f16_f32 v127, v36, v37
	ds_write_b16 v118, v120
	ds_write_b16_d16_hi v118, v120 offset:528
	ds_write_b16 v118, v121 offset:1056
	ds_write_b16_d16_hi v118, v121 offset:1584
	ds_write_b16 v118, v122 offset:32
	ds_write_b16_d16_hi v118, v122 offset:560
	ds_write_b16 v118, v123 offset:1088
	ds_write_b16_d16_hi v118, v123 offset:1616
	ds_write_b16 v118, v124 offset:256
	ds_write_b16_d16_hi v118, v124 offset:784
	ds_write_b16 v118, v125 offset:1312
	ds_write_b16_d16_hi v118, v125 offset:1840
	ds_write_b16 v118, v126 offset:288
	ds_write_b16_d16_hi v118, v126 offset:816
	ds_write_b16 v118, v127 offset:1344
	ds_write_b16_d16_hi v118, v127 offset:1872
.Lmy_qe3_end:
	s_add_i32 s53, s37, 112
	s_add_i32 s54, s53, s18
	s_lshr_b32 s55, s54, 10
	s_lshr_b32 s56, s53, 6
	s_mul_i32 s56, s56, 0x9000
	s_and_b32 s57, s53, 63
	v_pk_add_f32 v[30:31], v[204:205], v[30:31]
	v_pk_add_f32 v[32:33], v[206:207], v[32:33]
	v_pk_add_f32 v[26:27], v[204:205], v[26:27]
	v_pk_add_f32 v[28:29], v[206:207], v[28:29]
	v_pk_add_f32 v[22:23], v[204:205], v[22:23]
	v_pk_add_f32 v[24:25], v[206:207], v[24:25]
	v_pk_add_f32 v[18:19], v[204:205], v[18:19]
	v_pk_add_f32 v[20:21], v[206:207], v[20:21]
	s_cmp_eq_u32 s55, 2
	s_cbranch_scc1 .Lmy_qe4_v
	s_lshl_b32 s58, s57, 1
	s_add_i32 s58, s58, s56
	v_add_u32_e32 v118, s58, v113
	s_cmp_eq_u32 s55, 0
	s_cbranch_scc0 .Lmy_qe4_ns
	v_pk_mul_f32 v[30:31], v[116:117], v[30:31]
	v_pk_mul_f32 v[32:33], v[116:117], v[32:33]
	v_pk_mul_f32 v[26:27], v[116:117], v[26:27]
	v_pk_mul_f32 v[28:29], v[116:117], v[28:29]
	v_pk_mul_f32 v[22:23], v[116:117], v[22:23]
	v_pk_mul_f32 v[24:25], v[116:117], v[24:25]
	v_pk_mul_f32 v[18:19], v[116:117], v[18:19]
	v_pk_mul_f32 v[20:21], v[116:117], v[20:21]
.Lmy_qe4_ns:
	v_cvt_pk_f16_f32 v120, v30, v31
	v_cvt_pk_f16_f32 v121, v32, v33
	v_cvt_pk_f16_f32 v122, v26, v27
	v_cvt_pk_f16_f32 v123, v28, v29
	v_cvt_pk_f16_f32 v124, v22, v23
	v_cvt_pk_f16_f32 v125, v24, v25
	v_cvt_pk_f16_f32 v126, v18, v19
	v_cvt_pk_f16_f32 v127, v20, v21
	ds_write_b64 v118, v[120:121]
	ds_write_b64 v118, v[122:123] offset:2304
	ds_write_b64 v118, v[124:125] offset:18432
	ds_write_b64 v118, v[126:127] offset:20736
	s_branch .Lmy_qe4_end
.Lmy_qe4_v:
	s_mul_i32 s58, s57, 0x210
	s_add_i32 s58, s58, s56
	v_add_u32_e32 v118, s58, v114
	v_cvt_pk_f16_f32 v120, v30, v31
	v_cvt_pk_f16_f32 v121, v32, v33
	v_cvt_pk_f16_f32 v122, v26, v27
	v_cvt_pk_f16_f32 v123, v28, v29
	v_cvt_pk_f16_f32 v124, v22, v23
	v_cvt_pk_f16_f32 v125, v24, v25
	v_cvt_pk_f16_f32 v126, v18, v19
	v_cvt_pk_f16_f32 v127, v20, v21
	ds_write_b16 v118, v120
	ds_write_b16_d16_hi v118, v120 offset:528
	ds_write_b16 v118, v121 offset:1056
	ds_write_b16_d16_hi v118, v121 offset:1584
	ds_write_b16 v118, v122 offset:32
	ds_write_b16_d16_hi v118, v122 offset:560
	ds_write_b16 v118, v123 offset:1088
	ds_write_b16_d16_hi v118, v123 offset:1616
	ds_write_b16 v118, v124 offset:256
	ds_write_b16_d16_hi v118, v124 offset:784
	ds_write_b16 v118, v125 offset:1312
	ds_write_b16_d16_hi v118, v125 offset:1840
	ds_write_b16 v118, v126 offset:288
	ds_write_b16_d16_hi v118, v126 offset:816
	ds_write_b16 v118, v127 offset:1344
	ds_write_b16_d16_hi v118, v127 offset:1872
.Lmy_qe4_end:
	s_add_i32 s53, s37, 128
	s_add_i32 s54, s53, s18
	s_lshr_b32 s55, s54, 10
	s_lshr_b32 s56, s53, 6
	s_mul_i32 s56, s56, 0x9000
	s_and_b32 s57, s53, 63
	v_pk_add_f32 v[14:15], v[208:209], v[14:15]
	v_pk_add_f32 v[16:17], v[210:211], v[16:17]
	v_pk_add_f32 v[10:11], v[208:209], v[10:11]
	v_pk_add_f32 v[12:13], v[210:211], v[12:13]
	v_pk_add_f32 v[6:7], v[208:209], v[6:7]
	v_pk_add_f32 v[8:9], v[210:211], v[8:9]
	v_pk_add_f32 v[2:3], v[208:209], v[2:3]
	v_pk_add_f32 v[4:5], v[210:211], v[4:5]
	s_cmp_eq_u32 s55, 2
	s_cbranch_scc1 .Lmy_qe5_v
	s_lshl_b32 s58, s57, 1
	s_add_i32 s58, s58, s56
	v_add_u32_e32 v118, s58, v113
	s_cmp_eq_u32 s55, 0
	s_cbranch_scc0 .Lmy_qe5_ns
	v_pk_mul_f32 v[14:15], v[116:117], v[14:15]
	v_pk_mul_f32 v[16:17], v[116:117], v[16:17]
	v_pk_mul_f32 v[10:11], v[116:117], v[10:11]
	v_pk_mul_f32 v[12:13], v[116:117], v[12:13]
	v_pk_mul_f32 v[6:7], v[116:117], v[6:7]
	v_pk_mul_f32 v[8:9], v[116:117], v[8:9]
	v_pk_mul_f32 v[2:3], v[116:117], v[2:3]
	v_pk_mul_f32 v[4:5], v[116:117], v[4:5]
.Lmy_qe5_ns:
	v_cvt_pk_f16_f32 v120, v14, v15
	v_cvt_pk_f16_f32 v121, v16, v17
	v_cvt_pk_f16_f32 v122, v10, v11
	v_cvt_pk_f16_f32 v123, v12, v13
	v_cvt_pk_f16_f32 v124, v6, v7
	v_cvt_pk_f16_f32 v125, v8, v9
	v_cvt_pk_f16_f32 v126, v2, v3
	v_cvt_pk_f16_f32 v127, v4, v5
	ds_write_b64 v118, v[120:121]
	ds_write_b64 v118, v[122:123] offset:2304
	ds_write_b64 v118, v[124:125] offset:18432
	ds_write_b64 v118, v[126:127] offset:20736
	s_branch .Lmy_qe5_end
.Lmy_qe5_v:
	s_mul_i32 s58, s57, 0x210
	s_add_i32 s58, s58, s56
	v_add_u32_e32 v118, s58, v114
	v_cvt_pk_f16_f32 v120, v14, v15
	v_cvt_pk_f16_f32 v121, v16, v17
	v_cvt_pk_f16_f32 v122, v10, v11
	v_cvt_pk_f16_f32 v123, v12, v13
	v_cvt_pk_f16_f32 v124, v6, v7
	v_cvt_pk_f16_f32 v125, v8, v9
	v_cvt_pk_f16_f32 v126, v2, v3
	v_cvt_pk_f16_f32 v127, v4, v5
	ds_write_b16 v118, v120
	ds_write_b16_d16_hi v118, v120 offset:528
	ds_write_b16 v118, v121 offset:1056
	ds_write_b16_d16_hi v118, v121 offset:1584
	ds_write_b16 v118, v122 offset:32
	ds_write_b16_d16_hi v118, v122 offset:560
	ds_write_b16 v118, v123 offset:1088
	ds_write_b16_d16_hi v118, v123 offset:1616
	ds_write_b16 v118, v124 offset:256
	ds_write_b16_d16_hi v118, v124 offset:784
	ds_write_b16 v118, v125 offset:1312
	ds_write_b16_d16_hi v118, v125 offset:1840
	ds_write_b16 v118, v126 offset:288
	ds_write_b16_d16_hi v118, v126 offset:816
	ds_write_b16 v118, v127 offset:1344
	ds_write_b16_d16_hi v118, v127 offset:1872
.Lmy_qe5_end:
.LBB1_102:
	s_lshl_b32 s0, s36, 8
	s_lshr_b32 s12, s36, 3
	s_and_b32 s4, s0, 0x700
	s_lshl_b32 s5, s12, 21
	s_lshl_b32 s0, s4, 1
	s_add_u32 s0, s10, s0
	s_addc_u32 s1, s11, 0
	s_bfe_u32 s11, s18, 0x40006
	v_and_b32_e32 v4, 0x1f0, v1
	v_mov_b32_e32 v5, 0
	s_cmp_gt_i32 s33, 10
	v_lshl_add_u64 v[2:3], s[0:1], 0, v[4:5]
	s_cselect_b64 s[0:1], -1, 0
	s_mov_b32 s3, 0
	s_and_b64 vcc, exec, s[0:1]
	v_lshrrev_b32_e32 v10, 5, v0
	s_waitcnt lgkmcnt(0)
	s_barrier
	s_cbranch_vccz .LBB1_104
	s_lshl_b32 s2, s5, 1
	s_lshl_b32 s10, s11, 18
	s_or_b32 s2, s10, s2
	v_lshl_add_u64 v[8:9], v[2:3], 0, s[2:3]
	s_movk_i32 s2, 0x210
	v_lshlrev_b32_e32 v6, 12, v10
	v_mov_b32_e32 v7, v5
	v_mad_u32_u24 v11, v10, s2, v4
	v_lshl_add_u64 v[24:25], v[8:9], 0, v[6:7]
	v_or_b32_e32 v7, 0x200, v0
	ds_read_b128 v[12:15], v11
	v_lshrrev_b32_e32 v7, 5, v7
	v_mad_u32_u24 v16, v7, s2, v4
	ds_read_b128 v[16:19], v16
	ds_read_b128 v[20:23], v11 offset:16896
	v_or_b32_e32 v6, 0x20000, v6
	s_waitcnt lgkmcnt(2)
	global_store_dwordx4 v[24:25], v[12:15], off nt
	s_nop 1
	v_lshlrev_b32_e32 v12, 12, v7
	v_mov_b32_e32 v13, v5
	v_mov_b32_e32 v7, v5
	v_or_b32_e32 v5, 0x600, v0
	v_lshl_add_u64 v[12:13], v[8:9], 0, v[12:13]
	v_lshl_add_u64 v[6:7], v[8:9], 0, v[6:7]
	v_lshrrev_b32_e32 v5, 5, v5
	s_waitcnt lgkmcnt(1)
	global_store_dwordx4 v[12:13], v[16:19], off nt
	s_waitcnt lgkmcnt(0)
	global_store_dwordx4 v[6:7], v[20:23], off nt
	v_mad_u32_u24 v7, v5, s2, v4
	v_lshlrev_b32_e32 v6, 12, v5
	s_lshl_b32 s10, s12, 15
	v_and_b32_e32 v5, 0x70, v1
	s_cbranch_execz .LBB1_105
	s_branch .LBB1_106

.LBB1_105:
	s_cmpk_lt_u32 s18, 0x400
	s_cselect_b32 s3, s7, s9
	s_cselect_b32 s2, s6, s8
	s_lshl_b32 s11, s11, 11
	s_or_b32 s11, s10, s11
	s_or_b32 s11, s11, s4
	s_lshl_b32 s11, s11, 7
	v_or_b32_e32 v11, 0x200, v0
	s_add_u32 s2, s2, s11
	s_movk_i32 s11, 0x90
	v_lshrrev_b32_e32 v7, 3, v11
	v_or_b32_e32 v20, 0x400, v0
	v_mad_u32_u24 v6, v104, s11, v5
	v_mad_u32_u24 v12, v7, s11, v5
	v_lshrrev_b32_e32 v16, 3, v20
	ds_read_b128 v[6:9], v6
	ds_read_b128 v[12:15], v12
	v_mad_u32_u24 v16, v16, s11, v5
	ds_read_b128 v[16:19], v16
	s_addc_u32 s3, s3, 0
	s_waitcnt lgkmcnt(2)
	global_store_dwordx4 v1, v[6:9], s[2:3] nt
	s_nop 1
	v_lshlrev_b32_e32 v6, 4, v11
	s_waitcnt lgkmcnt(1)
	global_store_dwordx4 v6, v[12:15], s[2:3] nt
	v_lshlrev_b32_e32 v6, 4, v20
	s_waitcnt lgkmcnt(0)
	global_store_dwordx4 v6, v[16:19], s[2:3] nt
	v_or_b32_e32 v6, 0x600, v0
	v_lshrrev_b32_e32 v7, 3, v6
	v_mad_u32_u24 v7, v7, s11, v5
	v_lshlrev_b32_e32 v6, 4, v6
	v_mov_b64_e32 v[8:9], s[2:3]
.LBB1_106:
	ds_read_b128 v[12:15], v7
	v_mov_b32_e32 v7, 0
	s_add_i32 s2, s18, 64
	v_lshl_add_u64 v[8:9], v[8:9], 0, v[6:7]
	s_andn2_b64 vcc, exec, s[0:1]
	s_bfe_u32 s3, s2, 0x40006
	s_waitcnt lgkmcnt(0)
	global_store_dwordx4 v[8:9], v[12:15], off nt
	s_cbranch_vccnz .LBB1_108
	s_lshl_b32 s0, s5, 1
	s_lshl_b32 s1, s3, 18
	s_or_b32 s0, s1, s0
	s_mov_b32 s1, 0
	v_lshl_add_u64 v[8:9], v[2:3], 0, s[0:1]
	s_movk_i32 s0, 0x210
	v_mad_u32_u24 v11, v10, s0, v4
	v_or_b32_e32 v16, 0x200, v0
	ds_read_b128 v[12:15], v11 offset:36864
	v_lshrrev_b32_e32 v26, 5, v16
	v_mad_u32_u24 v16, v26, s0, v4
	ds_read_b128 v[16:19], v16 offset:36864
	ds_read_b128 v[20:23], v11 offset:53760
	v_lshlrev_b32_e32 v6, 12, v10
	v_lshl_add_u64 v[24:25], v[8:9], 0, v[6:7]
	s_waitcnt lgkmcnt(2)
	global_store_dwordx4 v[24:25], v[12:15], off nt
	v_or_b32_e32 v6, 0x20000, v6
	s_mov_b32 s0, 0x9000
	v_lshlrev_b32_e32 v12, 12, v26
	v_mov_b32_e32 v13, v7
	v_lshl_add_u64 v[12:13], v[8:9], 0, v[12:13]
	v_lshl_add_u64 v[6:7], v[8:9], 0, v[6:7]
	s_waitcnt lgkmcnt(1)
	global_store_dwordx4 v[12:13], v[16:19], off nt
	s_waitcnt lgkmcnt(0)
	global_store_dwordx4 v[6:7], v[20:23], off nt
	v_or_b32_e32 v6, 0x600, v0
	v_lshrrev_b32_e32 v6, 5, v6
	v_mul_u32_u24_e32 v7, 0x210, v6
	v_add3_u32 v7, v4, v7, s0
	v_lshlrev_b32_e32 v6, 12, v6
	s_cbranch_execz .LBB1_109
	s_branch .LBB1_110
.LBB1_108:
.LBB1_109:
	s_cmpk_lt_u32 s2, 0x400
	s_cselect_b32 s1, s7, s9
	s_cselect_b32 s0, s6, s8
	s_lshl_b32 s2, s3, 11
	s_or_b32 s2, s10, s2
	s_or_b32 s2, s2, s4
	s_lshl_b32 s2, s2, 7
	v_or_b32_e32 v11, 0x200, v0
	s_add_u32 s0, s0, s2
	s_movk_i32 s2, 0x90
	v_lshrrev_b32_e32 v7, 3, v11
	v_or_b32_e32 v20, 0x400, v0
	v_mad_u32_u24 v6, v104, s2, v5
	v_mad_u32_u24 v12, v7, s2, v5
	v_lshrrev_b32_e32 v16, 3, v20
	ds_read_b128 v[6:9], v6 offset:36864
	ds_read_b128 v[12:15], v12 offset:36864
	v_mad_u32_u24 v16, v16, s2, v5
	ds_read_b128 v[16:19], v16 offset:36864
	s_addc_u32 s1, s1, 0
	s_waitcnt lgkmcnt(2)
	global_store_dwordx4 v1, v[6:9], s[0:1] nt
	s_mov_b32 s2, 0x9000
	s_nop 0
	v_lshlrev_b32_e32 v6, 4, v11
	s_waitcnt lgkmcnt(1)
	global_store_dwordx4 v6, v[12:15], s[0:1] nt
	v_lshlrev_b32_e32 v6, 4, v20
	s_waitcnt lgkmcnt(0)
	global_store_dwordx4 v6, v[16:19], s[0:1] nt
	v_or_b32_e32 v6, 0x600, v0
	v_lshrrev_b32_e32 v7, 3, v6
	v_mul_u32_u24_e32 v7, 0x90, v7
	v_add3_u32 v7, v5, v7, s2
	v_lshlrev_b32_e32 v6, 4, v6
	v_mov_b64_e32 v[8:9], s[0:1]
.LBB1_110:
	ds_read_b128 v[12:15], v7
	s_addk_i32 s18, 0x80
	v_mov_b32_e32 v7, 0
	s_bfe_u32 s2, s18, 0x40006
	v_lshl_add_u64 v[8:9], v[8:9], 0, v[6:7]
	s_cmp_lt_i32 s33, 10
	s_waitcnt lgkmcnt(0)
	global_store_dwordx4 v[8:9], v[12:15], off nt
	s_cbranch_scc1 .LBB1_112
	s_lshl_b32 s0, s5, 1
	s_lshl_b32 s1, s2, 18
	s_or_b32 s0, s1, s0
	s_mov_b32 s1, 0
	v_or_b32_e32 v4, 0x12000, v4
	v_lshl_add_u64 v[2:3], v[2:3], 0, s[0:1]
	s_movk_i32 s0, 0x210
	v_mad_u32_u24 v16, v10, s0, v4
	v_or_b32_e32 v8, 0x200, v0
	ds_read_b128 v[12:15], v16
	v_lshrrev_b32_e32 v22, 5, v8
	v_mad_u32_u24 v8, v22, s0, v4
	v_lshlrev_b32_e32 v6, 12, v10
	ds_read_b128 v[8:11], v8
	ds_read_b128 v[16:19], v16 offset:16896
	v_lshl_add_u64 v[20:21], v[2:3], 0, v[6:7]
	s_waitcnt lgkmcnt(2)
	global_store_dwordx4 v[20:21], v[12:15], off nt
	v_or_b32_e32 v6, 0x20000, v6
	s_nop 0
	v_lshlrev_b32_e32 v12, 12, v22
	v_mov_b32_e32 v13, v7
	v_lshl_add_u64 v[12:13], v[2:3], 0, v[12:13]
	v_lshl_add_u64 v[6:7], v[2:3], 0, v[6:7]
	s_waitcnt lgkmcnt(1)
	global_store_dwordx4 v[12:13], v[8:11], off nt
	s_waitcnt lgkmcnt(0)
	global_store_dwordx4 v[6:7], v[16:19], off nt
	v_or_b32_e32 v6, 0x600, v0
	v_lshrrev_b32_e32 v7, 5, v6
	v_mad_u32_u24 v6, v7, s0, v4
	v_lshlrev_b32_e32 v4, 12, v7
	s_cbranch_execz .LBB1_113
	s_branch .LBB1_114
.LBB1_112:
.LBB1_113:
	s_cmpk_lt_u32 s18, 0x400
	s_cselect_b32 s1, s7, s9
	s_cselect_b32 s0, s6, s8
	s_lshl_b32 s2, s2, 11
	s_or_b32 s2, s10, s2
	s_or_b32 s2, s2, s4
	s_lshl_b32 s2, s2, 7
	v_or_b32_e32 v15, 0x200, v0
	s_add_u32 s0, s0, s2
	v_or_b32_e32 v14, 0x12000, v5
	s_movk_i32 s2, 0x90
	v_lshrrev_b32_e32 v3, 3, v15
	v_or_b32_e32 v16, 0x400, v0
	v_mad_u32_u24 v2, v104, s2, v14
	v_mad_u32_u24 v6, v3, s2, v14
	v_lshrrev_b32_e32 v10, 3, v16
	ds_read_b128 v[2:5], v2
	ds_read_b128 v[6:9], v6
	v_mad_u32_u24 v10, v10, s2, v14
	ds_read_b128 v[10:13], v10
	s_addc_u32 s1, s1, 0
	s_waitcnt lgkmcnt(2)
	global_store_dwordx4 v1, v[2:5], s[0:1] nt
	v_lshlrev_b32_e32 v1, 4, v15
	s_waitcnt lgkmcnt(1)
	global_store_dwordx4 v1, v[6:9], s[0:1] nt
	v_lshlrev_b32_e32 v1, 4, v16
	v_or_b32_e32 v0, 0x600, v0
	s_waitcnt lgkmcnt(0)
	global_store_dwordx4 v1, v[10:13], s[0:1] nt
	v_lshrrev_b32_e32 v1, 3, v0
	v_mad_u32_u24 v6, v1, s2, v14
	v_lshlrev_b32_e32 v4, 4, v0
	v_mov_b64_e32 v[2:3], s[0:1]
.LBB1_114:
	ds_read_b128 v[6:9], v6
	v_mov_b32_e32 v5, 0
	v_lshl_add_u64 v[0:1], v[2:3], 0, v[4:5]
	s_waitcnt lgkmcnt(0)
	global_store_dwordx4 v[0:1], v[6:9], off nt
	s_endpgm
